# c21 + odd workgroups run the prologue's row-conversion section before the weight-transpose section (overlap bandwidth-bound and latency-bound halves)
# speedup vs baseline: 1.2464x; 1.0022x over previous
; __global__ void __launch_bounds__(NTHREADS, 2) fwd(Args args) {
;     ...
;     if (IN(PH_PRO)) {
;         LAS float* scr = (LAS float*)(F.lds + RING_OFF + F.wave * 16384);
;         int off = 0;
;         for (int id = 0; id < 9; ++id) {
;             if (id == 2 || id == 3 || id == 4 || id == 5 || id == 8) continue;
;             const float* src; const float* gain = nullptr; bf16* dst = nullptr; int K, N, mode = 0;
;             {
;                 switch (id) {
;                     case 0: src = args.in[7]; dst = (bf16*)(ws + WS_WIN0); K = DM; N = N_IN0; gain = norm_mix_; break;
;                     case 1: src = args.in[9]; dst = (bf16*)(ws + WS_WMKV0); K = DM; N = 512; break;
;                     case 2: src = args.in[10]; dst = (bf16*)(ws + WS_WOUT0); K = DM; N = DM; break;
;                     case 3: src = args.in[14]; dst = (bf16*)(ws + WS_WGU0); K = DM; N = FF; mode = 1; gain = norm_ffn_; break;
;                     case 4: src = args.in[15]; dst = (bf16*)(ws + WS_WGU0); K = DM; N = FF; mode = 2; gain = norm_ffn_; break;
;                     case 5: src = args.in[16]; dst = (bf16*)(ws + WS_WD0); K = FF; N = DM; break;
;                     case 6: src = args.in[11]; dst = (bf16*)(ws + WS_WIN1); K = DM; N = N_IN1; gain = norm_mix_ + DM; break;
;                     case 7: src = args.in[12]; dst = (bf16*)(ws + WS_WMKV1); K = DM; N = 512; break;
;                     default: src = args.in[13]; dst = (bf16*)(ws + WS_WOUT1); K = 512; N = DM; break;
;                 }
;             }
;             const int nnb = N / 32, nit = (K / 64) * nnb;
;             int first = gw - off; if (first < 0) first += NGW;
;             for (int it = first; it < nit; it += NGW) { const int kb = it / nnb, nb = it % nnb, n0 = 32 * nb;
;                 const int drow0 = mode == 0 ? n0 : 256 * (n0 >> 7) + (n0 & 127) + (mode == 2 ? 128 : 0);
;                 if (id == 6 || id == 0 || id == 1 || id == 7) p0_transpose_item_f8(src, K, N, (unsigned char*)dst, drow0, 64 * kb, n0, 16.f, scr, F.lane, gain);
;                 else p0_transpose_item(src, K, N, dst, drow0, 64 * kb, n0, gain, scr, F.lane); }
;             off = (off + nit) % NGW;
;         }
;         { unsigned char* wz = ws + WS_WIN0 + (size_t)N_IN0 * DM;
;           for (int i = F.bid * NTHREADS + F.tid; i < (N_IN0P - N_IN0) * DM / 16; i += GRID * NTHREADS) ((GAS v4u*)wz)[i] = (v4u){0u, 0u, 0u, 0u}; }
.LBB0_12:
	s_or_b64 exec, exec, s[8:9]
	s_load_dwordx16 s[16:31], s[66:67], 0x0
	v_writelane_b32 v248, s66, 6
	s_lshr_b32 s82, s14, 6
	s_lshl_b32 s0, s2, 3
	v_writelane_b32 v248, s67, 7
	s_load_dwordx16 s[36:51], s[66:67], 0x40
	s_add_i32 s66, s82, s0
	s_cmp_lt_i32 s64, 1
	s_cselect_b64 s[4:5], -1, 0
	s_cmp_gt_i32 s65, 0
	s_cselect_b64 s[6:7], -1, 0
	s_and_b64 s[10:11], s[4:5], s[6:7]
	v_and_b32_e32 v162, 63, v0
	v_writelane_b32 v248, s0, 8
	s_mov_b32 s67, 0
	s_andn2_b64 vcc, exec, s[10:11]
	v_and_b32_e32 v164, 31, v0
	v_and_b32_e32 v1, 7, v0
	v_writelane_b32 v248, s82, 9
	s_cbranch_vccnz .LBB0_81
	s_mov_b32 s98, 0
	s_waitcnt lgkmcnt(0)
	s_bitcmp1_b32 s2, 0
	s_cbranch_scc1 .LBB0_70
.Lpro_weights:
	s_mov_b32 s67, 0
	s_lshl_b32 s3, s82, 14
	s_add_i32 s4, s3, 0
	s_add_u32 s8, s34, 0x800000
	s_addc_u32 s9, s35, 0
	s_add_u32 s12, s34, 0x2000000
	s_addc_u32 s13, s35, 0
	s_waitcnt lgkmcnt(0)
	s_add_u32 s14, s24, 0x1000
	s_addc_u32 s15, s25, 0
	s_add_u32 s70, s34, 0x1900000
	s_addc_u32 s71, s35, 0
	s_add_u32 s72, s34, 0xb00000
	s_addc_u32 s73, s35, 0
	s_add_u32 s74, s34, 0x900000
	s_addc_u32 s75, s35, 0
	s_add_u32 s76, s34, 0x700000
	s_addc_u32 s77, s35, 0
	v_lshrrev_b32_e32 v31, 3, v162
	s_add_u32 s78, s34, 0x400000
	v_lshrrev_b32_e32 v30, 5, v162
	v_mul_u32_u24_e32 v2, 0x420, v1
	v_lshlrev_b32_e32 v3, 2, v31
	s_addc_u32 s79, s35, 0
	v_add3_u32 v32, s4, v2, v3
	v_mul_u32_u24_e32 v2, 0x84, v30
	s_add_u32 s80, s34, 0x2500000
	v_mov_b32_e32 v11, 0
	v_lshlrev_b32_e32 v12, 3, v1
	v_or_b32_e32 v2, s3, v2
	v_lshlrev_b32_e32 v3, 2, v164
	s_addc_u32 s81, s35, 0
	v_mov_b32_e32 v13, v11
	v_or_b32_e32 v33, 8, v31
	v_or_b32_e32 v34, 16, v31
	v_or_b32_e32 v35, 24, v31
	v_add3_u32 v36, v2, v3, 0
	v_lshlrev_b32_e32 v10, 2, v164
	s_movk_i32 s83, 0x7fff
	s_mov_b32 s95, 0xffff0000
	s_mov_b32 s82, 0x41800000
	v_lshlrev_b32_e32 v14, 2, v12
	v_lshlrev_b32_e32 v16, 1, v12
	s_mov_b32 s96, 0
	s_branch .LBB0_16

; #define GAS __attribute__((address_space(1)))
; __global__ void __launch_bounds__(NTHREADS, 2) fwd(Args args) {
;     ...
;             off = (off + nit) % NGW;
;         }
;         { unsigned char* wz = ws + WS_WIN0 + (size_t)N_IN0 * DM;
;           for (int i = F.bid * NTHREADS + F.tid; i < (N_IN0P - N_IN0) * DM / 16; i += GRID * NTHREADS) ((GAS v4u*)wz)[i] = (v4u){0u, 0u, 0u, 0u}; }
;         for (int m = gw; m < NMEM; m += NGW) rms_row_f8(args.in[1] + (size_t)m * DM, args.in[3], (unsigned char*)MEMN + (size_t)m * DM, F.lane);
;         for (int m = gw; m < SEQ; m += NGW) raw_row(x_ + (size_t)m * DM, HN + (size_t)m * DM, HN8A + (size_t)m * DM, SS1 + (size_t)m * 4, F.lane);
.Lpro_after_weights:
	v_readlane_b32 s82, v248, 9
	s_cmp_eq_u32 s98, 1
	s_cbranch_scc1 .LBB0_81

; __global__ void __launch_bounds__(NTHREADS, 2) fwd(Args args) {
;     ...
;         for (int m = gw; m < NMEM; m += NGW) rms_row_f8(args.in[1] + (size_t)m * DM, args.in[3], (unsigned char*)MEMN + (size_t)m * DM, F.lane);
;         for (int m = gw; m < SEQ; m += NGW) raw_row(x_ + (size_t)m * DM, HN + (size_t)m * DM, HN8A + (size_t)m * DM, SS1 + (size_t)m * 4, F.lane);
;     }
.Lpro_rows_done:
	s_mov_b32 s98, 1
	s_bitcmp1_b32 s2, 0
	s_cbranch_scc1 .Lpro_weights

; #define LAS __attribute__((address_space(3)))
; __global__ void __launch_bounds__(NTHREADS, 2) fwd(Args args) {
;     extern __shared__ __attribute__((aligned(16))) unsigned char lds[];
;     Frame F;
;     F.lds = (LAS unsigned char*)lds; F.MISC = (volatile LAS unsigned*)(F.lds + MISC_OFF);
;     F.tid = threadIdx.x; F.lane = F.tid & 63; F.wave = __builtin_amdgcn_readfirstlane(F.tid >> 6); F.bid = blockIdx.x;
	.amdhsa_kernel _Z3fwd4Args
		.amdhsa_group_segment_fixed_size 0
		.amdhsa_private_segment_fixed_size 0
		.amdhsa_kernarg_size 448
		.amdhsa_user_sgpr_count 2
		.amdhsa_user_sgpr_dispatch_ptr 0
		.amdhsa_user_sgpr_queue_ptr 0
		.amdhsa_user_sgpr_kernarg_segment_ptr 1
		.amdhsa_user_sgpr_dispatch_id 0
		.amdhsa_user_sgpr_kernarg_preload_length 0
		.amdhsa_user_sgpr_kernarg_preload_offset 0
		.amdhsa_user_sgpr_private_segment_size 0
		.amdhsa_uses_dynamic_stack 0
		.amdhsa_enable_private_segment 0
		.amdhsa_system_sgpr_workgroup_id_x 1
		.amdhsa_system_sgpr_workgroup_id_y 0
		.amdhsa_system_sgpr_workgroup_id_z 0
		.amdhsa_system_sgpr_workgroup_info 0
		.amdhsa_system_vgpr_workitem_id 0
		.amdhsa_next_free_vgpr 249
		.amdhsa_next_free_sgpr 99
		.amdhsa_accum_offset 252
		.amdhsa_reserve_vcc 1
		.amdhsa_float_round_mode_32 0
		.amdhsa_float_round_mode_16_64 0
		.amdhsa_float_denorm_mode_32 3
		.amdhsa_float_denorm_mode_16_64 3
		.amdhsa_dx10_clamp 1
		.amdhsa_ieee_mode 1
		.amdhsa_fp16_overflow 0
		.amdhsa_tg_split 0
		.amdhsa_exception_fp_ieee_invalid_op 0
		.amdhsa_exception_fp_denorm_src 0
		.amdhsa_exception_fp_ieee_div_zero 0
		.amdhsa_exception_fp_ieee_overflow 0
		.amdhsa_exception_fp_ieee_underflow 0
		.amdhsa_exception_fp_ieee_inexact 0
		.amdhsa_exception_int_div_zero 0
	.end_amdhsa_kernel

; #define LAS __attribute__((address_space(3)))
; __global__ void __launch_bounds__(NTHREADS, 2) fwd(Args args) {
;     extern __shared__ __attribute__((aligned(16))) unsigned char lds[];
;     Frame F;
;     F.lds = (LAS unsigned char*)lds; F.MISC = (volatile LAS unsigned*)(F.lds + MISC_OFF);
;     F.tid = threadIdx.x; F.lane = F.tid & 63; F.wave = __builtin_amdgcn_readfirstlane(F.tid >> 6); F.bid = blockIdx.x;
amdhsa.kernels:
  - .agpr_count:     0
    .args:
      - .offset:         0
        .size:           192
        .value_kind:     by_value
      - .offset:         192
        .size:           4
        .value_kind:     hidden_block_count_x
      - .offset:         196
        .size:           4
        .value_kind:     hidden_block_count_y
      - .offset:         200
        .size:           4
        .value_kind:     hidden_block_count_z
      - .offset:         204
        .size:           2
        .value_kind:     hidden_group_size_x
      - .offset:         206
        .size:           2
        .value_kind:     hidden_group_size_y
      - .offset:         208
        .size:           2
        .value_kind:     hidden_group_size_z
      - .offset:         210
        .size:           2
        .value_kind:     hidden_remainder_x
      - .offset:         212
        .size:           2
        .value_kind:     hidden_remainder_y
      - .offset:         214
        .size:           2
        .value_kind:     hidden_remainder_z
      - .offset:         232
        .size:           8
        .value_kind:     hidden_global_offset_x
      - .offset:         240
        .size:           8
        .value_kind:     hidden_global_offset_y
      - .offset:         248
        .size:           8
        .value_kind:     hidden_global_offset_z
      - .offset:         256
        .size:           2
        .value_kind:     hidden_grid_dims
      - .offset:         312
        .size:           4
        .value_kind:     hidden_dynamic_lds_size
    .group_segment_fixed_size: 0
    .kernarg_segment_align: 8
    .kernarg_segment_size: 448
    .language:       OpenCL C
    .language_version:
      - 2
      - 0
    .max_flat_workgroup_size: 512
    .name:           _Z3fwd4Args
    .private_segment_fixed_size: 0
    .sgpr_count:     105
    .sgpr_spill_count: 10
    .symbol:         _Z3fwd4Args.kd
    .uniform_work_group_size: 1
    .uses_dynamic_stack: false
    .vgpr_count:     249
    .vgpr_spill_count: 0
    .wavefront_size: 64
